# v7 + attention loops: hipcc DMA_WAIT branch ladder deleted (8 sites, subsumed by vmcnt(0) before barrier); diff K reads use slot-0 address VGPRs with immediate slot offsets
# speedup vs baseline: 1.0074x; 1.0031x over previous
; #define DMA_WAIT(last) do { if (last) asm volatile("s_waitcnt vmcnt(0)" ::: "memory"); else asm volatile("s_waitcnt vmcnt(%0)" :: "n"(NPW) : "memory"); } while (0)
; template <int DK, int DV, bool OFF, class QLoader> ...
;     ...
;   f32x16 pA0, pA1, pB0, pB1; bf16x8 pa0, pa1, pa2, pa3; const int NT = nkeys / KVBLK;
;   DMA_TILE(0, 0); DMA_TILE(1, 1); DMA_WAIT(false); __syncthreads(); if (2 < NT) DMA_TILE(2, 2);
;   qkt<DK>(pA0, pA1, K_lds, qr, r32, hi); partialSM<DK, OFF>(pA0, pA1, negMC);
.LBB0_844:
.LBB0_846:
	s_add_i32 s28, s55, -3
	s_cmp_lt_u32 s28, s95
	s_cselect_b64 s[24:25], -1, 0
	s_cmp_ge_u32 s28, s95
	s_cselect_b64 s[28:29], -1, 0
	s_and_b64 vcc, exec, s[28:29]
	s_waitcnt vmcnt(0)
	s_barrier
	s_cbranch_vccnz .LBB0_856
	s_cmp_gt_u32 s57, 1
	s_cselect_b64 s[36:37], -1, 0
	s_mov_b64 s[38:39], -1
	s_and_b64 vcc, exec, s[36:37]
	s_cbranch_vccz .LBB0_851
	s_lshl_b64 s[30:31], s[2:3], 7
	s_add_u32 s30, s93, s30
	s_addc_u32 s31, s94, s31
	s_cbranch_execz .LBB0_852

; template <int DK>
; __device__ __forceinline__ void qkt(f32x16& p0, f32x16& p1, const char* Ks, const bf16x8* qr, int r32, int hi) {
;   p0 = f32x16{}; p1 = f32x16{};
; #pragma unroll
;   for (int d0 = 0; d0 < DK / 16; ++d0) { const int cb = (d0 * 16 + hi * 8) * 2;
;     const bf16x8 b0 = *reinterpret_cast<const bf16x8*>(Ks + ATT_KSWZ(r32, cb));
;     const bf16x8 b1 = *reinterpret_cast<const bf16x8*>(Ks + ATT_KSWZ(32 + r32, cb));
;     p0 = __builtin_amdgcn_mfma_f32_32x32x16_bf16(b0, qr[d0], p0, 0, 0, 0);
;     p1 = __builtin_amdgcn_mfma_f32_32x32x16_bf16(b1, qr[d0], p1, 0, 0, 0);
;   }
; }
.LBB0_856:
	ds_read_b128 v[82:85], v162 offset:16384
	ds_read_b128 v[86:89], v162 offset:24576
	ds_read_b128 v[130:133], v164 offset:16384
	ds_read_b128 v[134:137], v164 offset:24576
	v_exp_f32_e32 v66, v66
	v_add_f32_e32 v180, 0, v173
	v_add_f32_e32 v180, v174, v180
	v_add_f32_e32 v180, v175, v180
	v_add_f32_e32 v180, v184, v180
	v_add_f32_e32 v180, v185, v180
	v_add_f32_e32 v180, v186, v180
	v_add_f32_e32 v180, v187, v180
	v_add_f32_e32 v180, v188, v180
	v_add_f32_e32 v180, v189, v180
	v_add_f32_e32 v180, v190, v180
	v_add_f32_e32 v180, v191, v180
	v_add_f32_e32 v180, v192, v180
	v_add_f32_e32 v180, v193, v180
	v_add_f32_e32 v180, v194, v180
	v_add_f32_e32 v180, v195, v180
	v_add_f32_e32 v180, v196, v180
	s_waitcnt lgkmcnt(0)
	v_mfma_f32_32x32x16_bf16 v[98:113], v[82:85], v[114:117], 0
	v_exp_f32_e32 v67, v67
	v_exp_f32_e32 v68, v68
	v_exp_f32_e32 v69, v69
	v_exp_f32_e32 v70, v70
	v_exp_f32_e32 v71, v71
	v_exp_f32_e32 v72, v72
	v_exp_f32_e32 v73, v73
	v_mfma_f32_32x32x16_bf16 v[82:97], v[86:89], v[114:117], 0
	v_exp_f32_e32 v74, v74
	v_exp_f32_e32 v75, v75
	v_exp_f32_e32 v76, v76
	v_exp_f32_e32 v77, v77
	v_exp_f32_e32 v78, v78
	v_exp_f32_e32 v79, v79
	v_exp_f32_e32 v80, v80
	v_mfma_f32_32x32x16_bf16 v[98:113], v[130:133], v[118:121], v[98:113]
	v_exp_f32_e32 v81, v81
	s_andn2_b64 vcc, exec, s[26:27]
	v_mfma_f32_32x32x16_bf16 v[82:97], v[134:137], v[118:121], v[82:97]
	ds_read_b128 v[130:133], v166 offset:16384
	ds_read_b128 v[134:137], v166 offset:24576
	v_add_f32_e32 v180, v66, v180
	v_add_f32_e32 v180, v67, v180
	v_add_f32_e32 v180, v68, v180
	v_add_f32_e32 v180, v69, v180
	v_add_f32_e32 v180, v70, v180
	v_add_f32_e32 v180, v71, v180
	v_add_f32_e32 v180, v72, v180
	v_add_f32_e32 v180, v73, v180
	s_waitcnt lgkmcnt(0)
	v_mfma_f32_32x32x16_bf16 v[98:113], v[130:133], v[122:125], v[98:113]
	v_mfma_f32_32x32x16_bf16 v[82:97], v[134:137], v[122:125], v[82:97]
	ds_read_b128 v[130:133], v168 offset:16384
	ds_read_b128 v[134:137], v168 offset:24576
	v_add_f32_e32 v180, v74, v180
	v_add_f32_e32 v180, v75, v180
	v_add_f32_e32 v180, v76, v180
	v_add_f32_e32 v180, v77, v180
	v_add_f32_e32 v180, v78, v180
	v_add_f32_e32 v180, v79, v180
	v_add_f32_e32 v180, v80, v180
	v_add_f32_e32 v180, v81, v180
	s_waitcnt lgkmcnt(0)
	v_mfma_f32_32x32x16_bf16 v[98:113], v[130:133], v[126:129], v[98:113]
	v_mfma_f32_32x32x16_bf16 v[82:97], v[134:137], v[126:129], v[82:97]
	v_add_f32_e32 v172, v172, v180
	v_cvt_pk_bf16_f32 v130, v173, v174
	v_cvt_pk_bf16_f32 v131, v175, v184
	v_cvt_pk_bf16_f32 v132, v185, v186
	v_cvt_pk_bf16_f32 v133, v187, v188
	v_cvt_pk_bf16_f32 v134, v189, v190
	v_cvt_pk_bf16_f32 v135, v191, v192
	v_cvt_pk_bf16_f32 v136, v193, v194
	v_cvt_pk_bf16_f32 v137, v195, v196
	v_cvt_pk_bf16_f32 v138, v66, v67
	v_cvt_pk_bf16_f32 v139, v68, v69
	v_cvt_pk_bf16_f32 v140, v70, v71
	v_cvt_pk_bf16_f32 v141, v72, v73
	v_cvt_pk_bf16_f32 v142, v74, v75
	v_cvt_pk_bf16_f32 v143, v76, v77
	v_cvt_pk_bf16_f32 v144, v78, v79
	v_cvt_pk_bf16_f32 v145, v80, v81
	ds_read_b64_tr_b16 v[176:177], v169 offset:0
	ds_read_b64_tr_b16 v[178:179], v169 offset:0x800
	ds_read_b64_tr_b16 v[198:199], v169 offset:0x1000
	ds_read_b64_tr_b16 v[200:201], v169 offset:0x1800
	ds_read_b64_tr_b16 v[202:203], v169 offset:0x2000
	ds_read_b64_tr_b16 v[204:205], v169 offset:0x2800
	ds_read_b64_tr_b16 v[206:207], v169 offset:0x3000
	ds_read_b64_tr_b16 v[208:209], v169 offset:0x3800
	ds_read_b64_tr_b16 v[210:211], v169 offset:0x200
	ds_read_b64_tr_b16 v[212:213], v169 offset:0xa00
	ds_read_b64_tr_b16 v[214:215], v169 offset:0x1200
	s_nop 0
	v_permlane32_swap_b32_e32 v130, v132
	v_permlane32_swap_b32_e32 v131, v133
	ds_read_b64_tr_b16 v[216:217], v169 offset:0x1a00
	ds_read_b64_tr_b16 v[218:219], v169 offset:0x2200
	ds_read_b64_tr_b16 v[220:221], v169 offset:0x2a00
	ds_read_b64_tr_b16 v[222:223], v169 offset:0x3200
	ds_read_b64_tr_b16 v[224:225], v169 offset:0x3a00
	s_waitcnt lgkmcnt(8)
	v_permlane32_swap_b32_e32 v134, v136
	s_nop 0
	v_mfma_f32_32x32x16_bf16 v[2:17], v[130:133], v[176:179], v[2:17]
	v_permlane32_swap_b32_e32 v135, v137
	v_permlane32_swap_b32_e32 v138, v140
	v_permlane32_swap_b32_e32 v139, v141
	ds_read_b64_tr_b16 v[176:177], v169 offset:0x400
	v_mfma_f32_32x32x16_bf16 v[2:17], v[134:137], v[198:201], v[2:17]
	v_permlane32_swap_b32_e32 v142, v144
	v_permlane32_swap_b32_e32 v143, v145
	ds_read_b64_tr_b16 v[178:179], v169 offset:0xc00
	ds_read_b64_tr_b16 v[198:199], v169 offset:0x1400
	ds_read_b64_tr_b16 v[200:201], v169 offset:0x1c00
	v_mfma_f32_32x32x16_bf16 v[2:17], v[138:141], v[202:205], v[2:17]
	ds_read_b64_tr_b16 v[202:203], v169 offset:0x2400
	ds_read_b64_tr_b16 v[204:205], v169 offset:0x2c00
	v_exp_f32_e32 v197, v98
	v_mfma_f32_32x32x16_bf16 v[2:17], v[142:145], v[206:209], v[2:17]
	ds_read_b64_tr_b16 v[206:207], v169 offset:0x3400
	ds_read_b64_tr_b16 v[208:209], v169 offset:0x3c00
	s_waitcnt lgkmcnt(8)
	s_nop 0
	v_mfma_f32_32x32x16_bf16 v[50:65], v[130:133], v[210:213], v[50:65]
	ds_read_b64_tr_b16 v[210:211], v169 offset:0x600
	ds_read_b64_tr_b16 v[212:213], v169 offset:0xe00
	v_mfma_f32_32x32x16_bf16 v[50:65], v[134:137], v[214:217], v[50:65]
	ds_read_b64_tr_b16 v[214:215], v169 offset:0x1600
	ds_read_b64_tr_b16 v[216:217], v169 offset:0x1e00
	v_mfma_f32_32x32x16_bf16 v[50:65], v[138:141], v[218:221], v[50:65]
	ds_read_b64_tr_b16 v[218:219], v169 offset:0x2600
	ds_read_b64_tr_b16 v[220:221], v169 offset:0x2e00
	v_mfma_f32_32x32x16_bf16 v[50:65], v[142:145], v[222:225], v[50:65]
	ds_read_b64_tr_b16 v[222:223], v169 offset:0x3600
	ds_read_b64_tr_b16 v[224:225], v169 offset:0x3e00
	s_waitcnt lgkmcnt(8)
	s_nop 0
	s_waitcnt lgkmcnt(0)
	v_mfma_f32_32x32x16_bf16 v[34:49], v[130:133], v[176:179], v[34:49]
	v_mfma_f32_32x32x16_bf16 v[18:33], v[130:133], v[210:213], v[18:33]
	v_exp_f32_e32 v210, v105
	v_exp_f32_e32 v211, v111
	v_exp_f32_e32 v212, v113
	v_mfma_f32_32x32x16_bf16 v[34:49], v[134:137], v[198:201], v[34:49]
	v_exp_f32_e32 v200, v99
	v_exp_f32_e32 v198, v100
	v_exp_f32_e32 v199, v106
	v_exp_f32_e32 v201, v108
	v_mfma_f32_32x32x16_bf16 v[18:33], v[134:137], v[214:217], v[18:33]
	v_mfma_f32_32x32x16_bf16 v[34:49], v[138:141], v[202:205], v[34:49]
	v_exp_f32_e32 v202, v101
	v_exp_f32_e32 v204, v102
	v_exp_f32_e32 v205, v104
	v_exp_f32_e32 v203, v107
	v_mfma_f32_32x32x16_bf16 v[18:33], v[138:141], v[218:221], v[18:33]
	v_mfma_f32_32x32x16_bf16 v[34:49], v[142:145], v[206:209], v[34:49]
	v_exp_f32_e32 v207, v103
	v_exp_f32_e32 v209, v109
	v_exp_f32_e32 v206, v110
	v_exp_f32_e32 v208, v112
	v_mfma_f32_32x32x16_bf16 v[18:33], v[142:145], v[222:225], v[18:33]
	s_cbranch_vccnz .LBB0_865
; #define DMA_WAIT(last) do { if (last) asm volatile("s_waitcnt vmcnt(0)" ::: "memory"); else asm volatile("s_waitcnt vmcnt(%0)" :: "n"(NPW) : "memory"); } while (0)
; template <int DK, int DV, bool OFF, class QLoader> ...
;     ...
;   f32x16 pA0, pA1, pB0, pB1; bf16x8 pa0, pa1, pa2, pa3; const int NT = nkeys / KVBLK;
;   DMA_TILE(0, 0); DMA_TILE(1, 1); DMA_WAIT(false); __syncthreads(); if (2 < NT) DMA_TILE(2, 2);
;   qkt<DK>(pA0, pA1, K_lds, qr, r32, hi); partialSM<DK, OFF>(pA0, pA1, negMC);
.LBB0_859:
.LBB0_861:
	s_add_i32 s26, s55, -2
	s_cmp_ge_u32 s26, s95
	s_waitcnt vmcnt(0)
	s_barrier
	s_cbranch_scc1 .LBB0_863
	v_lshl_add_u64 v[66:67], v[156:157], 0, s[8:9]
	s_mov_b64 s[26:27], 0x1ec08000
	s_mov_b32 m0, s81
	v_lshl_add_u64 v[66:67], v[66:67], 0, s[26:27]
	global_load_lds_dwordx4 v[66:67], off
	v_lshl_add_u64 v[66:67], v[154:155], 0, s[8:9]
	s_mov_b64 s[26:27], 0x1ec08200
	v_lshl_add_u64 v[66:67], v[66:67], 0, s[26:27]
	s_mov_b32 m0, s83
	s_mov_b64 s[26:27], 0xdc01000
	global_load_lds_dwordx4 v[66:67], off
	v_lshl_add_u64 v[66:67], v[152:153], 0, s[8:9]
	v_lshl_add_u64 v[68:69], v[66:67], 0, s[26:27]
	s_mov_b32 m0, s82
	s_mov_b64 s[26:27], 0xdc01080
	global_load_lds_dwordx4 v[68:69], off
	v_lshl_add_u64 v[66:67], v[66:67], 0, s[26:27]
	s_mov_b32 m0, s84
	s_nop 0
	global_load_lds_dwordx4 v[66:67], off
; template <int DK>
; __device__ __forceinline__ void qkt(f32x16& p0, f32x16& p1, const char* Ks, const bf16x8* qr, int r32, int hi) {
;   p0 = f32x16{}; p1 = f32x16{};
; #pragma unroll
;   for (int d0 = 0; d0 < DK / 16; ++d0) { const int cb = (d0 * 16 + hi * 8) * 2;
;     const bf16x8 b0 = *reinterpret_cast<const bf16x8*>(Ks + ATT_KSWZ(r32, cb));
;     const bf16x8 b1 = *reinterpret_cast<const bf16x8*>(Ks + ATT_KSWZ(32 + r32, cb));
;     p0 = __builtin_amdgcn_mfma_f32_32x32x16_bf16(b0, qr[d0], p0, 0, 0, 0);
;     p1 = __builtin_amdgcn_mfma_f32_32x32x16_bf16(b1, qr[d0], p1, 0, 0, 0);
;   }
; }
.LBB0_863:
	ds_read_b128 v[66:69], v162 offset:32768
	ds_read_b128 v[70:73], v162 offset:40960
	ds_read_b128 v[130:133], v164 offset:32768
	ds_read_b128 v[134:137], v164 offset:40960
	v_exp_f32_e32 v82, v82
	v_add_f32_e32 v180, 0, v197
	v_add_f32_e32 v180, v200, v180
	v_add_f32_e32 v180, v198, v180
	v_add_f32_e32 v180, v202, v180
	v_add_f32_e32 v180, v204, v180
	v_add_f32_e32 v180, v207, v180
	v_add_f32_e32 v180, v205, v180
	v_add_f32_e32 v180, v210, v180
	v_add_f32_e32 v180, v199, v180
	v_add_f32_e32 v180, v203, v180
	v_add_f32_e32 v180, v201, v180
	v_add_f32_e32 v180, v209, v180
	v_add_f32_e32 v180, v206, v180
	v_add_f32_e32 v180, v211, v180
	v_add_f32_e32 v180, v208, v180
	v_add_f32_e32 v180, v212, v180
	s_waitcnt lgkmcnt(0)
	v_mfma_f32_32x32x16_bf16 v[98:113], v[66:69], v[114:117], 0
	v_exp_f32_e32 v83, v83
	v_exp_f32_e32 v84, v84
	v_exp_f32_e32 v85, v85
	v_exp_f32_e32 v86, v86
	v_exp_f32_e32 v87, v87
	v_exp_f32_e32 v88, v88
	v_exp_f32_e32 v89, v89
	v_mfma_f32_32x32x16_bf16 v[66:81], v[70:73], v[114:117], 0
	v_exp_f32_e32 v90, v90
	v_exp_f32_e32 v91, v91
	v_exp_f32_e32 v92, v92
	v_exp_f32_e32 v93, v93
	v_exp_f32_e32 v94, v94
	v_exp_f32_e32 v95, v95
	v_exp_f32_e32 v96, v96
	v_mfma_f32_32x32x16_bf16 v[98:113], v[130:133], v[118:121], v[98:113]
	v_exp_f32_e32 v97, v97
	v_mfma_f32_32x32x16_bf16 v[66:81], v[134:137], v[118:121], v[66:81]
	ds_read_b128 v[130:133], v166 offset:32768
	ds_read_b128 v[134:137], v166 offset:40960
	v_add_f32_e32 v180, v82, v180
	v_add_f32_e32 v180, v83, v180
	v_add_f32_e32 v180, v84, v180
	v_add_f32_e32 v180, v85, v180
	v_add_f32_e32 v180, v86, v180
	v_add_f32_e32 v180, v87, v180
	v_add_f32_e32 v180, v88, v180
	v_add_f32_e32 v180, v89, v180
	s_waitcnt lgkmcnt(0)
	v_mfma_f32_32x32x16_bf16 v[98:113], v[130:133], v[122:125], v[98:113]
	v_mfma_f32_32x32x16_bf16 v[66:81], v[134:137], v[122:125], v[66:81]
	ds_read_b128 v[130:133], v168 offset:32768
	ds_read_b128 v[134:137], v168 offset:40960
	v_add_f32_e32 v180, v90, v180
	v_add_f32_e32 v180, v91, v180
	v_add_f32_e32 v180, v92, v180
	v_add_f32_e32 v180, v93, v180
	v_add_f32_e32 v180, v94, v180
	v_add_f32_e32 v180, v95, v180
	v_add_f32_e32 v180, v96, v180
	v_add_f32_e32 v180, v97, v180
	s_waitcnt lgkmcnt(0)
	v_mfma_f32_32x32x16_bf16 v[98:113], v[130:133], v[126:129], v[98:113]
	v_mfma_f32_32x32x16_bf16 v[66:81], v[134:137], v[126:129], v[66:81]
	v_add_f32_e32 v172, v172, v180
	v_cvt_pk_bf16_f32 v130, v197, v200
	v_cvt_pk_bf16_f32 v131, v198, v202
	v_cvt_pk_bf16_f32 v132, v204, v207
	v_cvt_pk_bf16_f32 v133, v205, v210
	v_cvt_pk_bf16_f32 v134, v199, v203
	v_cvt_pk_bf16_f32 v135, v201, v209
	v_cvt_pk_bf16_f32 v136, v206, v211
	v_cvt_pk_bf16_f32 v137, v208, v212
	v_cvt_pk_bf16_f32 v138, v82, v83
	v_cvt_pk_bf16_f32 v139, v84, v85
	v_cvt_pk_bf16_f32 v140, v86, v87
	v_cvt_pk_bf16_f32 v141, v88, v89
	v_cvt_pk_bf16_f32 v142, v90, v91
	v_cvt_pk_bf16_f32 v143, v92, v93
	v_cvt_pk_bf16_f32 v144, v94, v95
	v_cvt_pk_bf16_f32 v145, v96, v97
	ds_read_b64_tr_b16 v[174:175], v170 offset:0
	ds_read_b64_tr_b16 v[176:177], v170 offset:0x800
	ds_read_b64_tr_b16 v[184:185], v170 offset:0x1000
	ds_read_b64_tr_b16 v[186:187], v170 offset:0x1800
	ds_read_b64_tr_b16 v[188:189], v170 offset:0x2000
	ds_read_b64_tr_b16 v[190:191], v170 offset:0x2800
	ds_read_b64_tr_b16 v[192:193], v170 offset:0x3000
	ds_read_b64_tr_b16 v[194:195], v170 offset:0x3800
	ds_read_b64_tr_b16 v[214:215], v170 offset:0x200
	ds_read_b64_tr_b16 v[216:217], v170 offset:0xa00
	ds_read_b64_tr_b16 v[218:219], v170 offset:0x1200
	s_nop 0
	v_permlane32_swap_b32_e32 v130, v132
	v_permlane32_swap_b32_e32 v131, v133
	ds_read_b64_tr_b16 v[220:221], v170 offset:0x1a00
	ds_read_b64_tr_b16 v[222:223], v170 offset:0x2200
	ds_read_b64_tr_b16 v[224:225], v170 offset:0x2a00
	ds_read_b64_tr_b16 v[226:227], v170 offset:0x3200
	ds_read_b64_tr_b16 v[228:229], v170 offset:0x3a00
	s_waitcnt lgkmcnt(8)
	v_permlane32_swap_b32_e32 v134, v136
	s_nop 0
	v_mfma_f32_32x32x16_bf16 v[2:17], v[130:133], v[174:177], v[2:17]
	v_permlane32_swap_b32_e32 v135, v137
	v_permlane32_swap_b32_e32 v138, v140
	v_permlane32_swap_b32_e32 v139, v141
	ds_read_b64_tr_b16 v[174:175], v170 offset:0x400
	v_mfma_f32_32x32x16_bf16 v[2:17], v[134:137], v[184:187], v[2:17]
	v_permlane32_swap_b32_e32 v142, v144
	v_permlane32_swap_b32_e32 v143, v145
	ds_read_b64_tr_b16 v[176:177], v170 offset:0xc00
	ds_read_b64_tr_b16 v[184:185], v170 offset:0x1400
	ds_read_b64_tr_b16 v[186:187], v170 offset:0x1c00
	v_mfma_f32_32x32x16_bf16 v[2:17], v[138:141], v[188:191], v[2:17]
	ds_read_b64_tr_b16 v[188:189], v170 offset:0x2400
	ds_read_b64_tr_b16 v[190:191], v170 offset:0x2c00
	v_exp_f32_e32 v173, v98
	v_exp_f32_e32 v196, v113
	v_mfma_f32_32x32x16_bf16 v[2:17], v[142:145], v[192:195], v[2:17]
	ds_read_b64_tr_b16 v[192:193], v170 offset:0x3400
	ds_read_b64_tr_b16 v[194:195], v170 offset:0x3c00
	s_waitcnt lgkmcnt(8)
	s_nop 0
	v_mfma_f32_32x32x16_bf16 v[50:65], v[130:133], v[214:217], v[50:65]
	ds_read_b64_tr_b16 v[214:215], v170 offset:0x600
	ds_read_b64_tr_b16 v[216:217], v170 offset:0xe00
	v_mfma_f32_32x32x16_bf16 v[50:65], v[134:137], v[218:221], v[50:65]
	ds_read_b64_tr_b16 v[218:219], v170 offset:0x1600
	ds_read_b64_tr_b16 v[220:221], v170 offset:0x1e00
	v_mfma_f32_32x32x16_bf16 v[50:65], v[138:141], v[222:225], v[50:65]
	ds_read_b64_tr_b16 v[222:223], v170 offset:0x2600
	ds_read_b64_tr_b16 v[224:225], v170 offset:0x2e00
	v_mfma_f32_32x32x16_bf16 v[50:65], v[142:145], v[226:229], v[50:65]
	ds_read_b64_tr_b16 v[226:227], v170 offset:0x3600
	ds_read_b64_tr_b16 v[228:229], v170 offset:0x3e00
	s_waitcnt lgkmcnt(8)
	s_nop 0
	s_waitcnt lgkmcnt(0)
	v_mfma_f32_32x32x16_bf16 v[34:49], v[130:133], v[174:177], v[34:49]
	v_exp_f32_e32 v174, v99
	v_exp_f32_e32 v175, v100
	v_mfma_f32_32x32x16_bf16 v[18:33], v[130:133], v[214:217], v[18:33]
	v_mfma_f32_32x32x16_bf16 v[34:49], v[134:137], v[184:187], v[34:49]
	v_exp_f32_e32 v184, v101
	v_exp_f32_e32 v185, v102
	v_exp_f32_e32 v186, v103
	v_exp_f32_e32 v187, v104
	v_mfma_f32_32x32x16_bf16 v[18:33], v[134:137], v[218:221], v[18:33]
	v_mfma_f32_32x32x16_bf16 v[34:49], v[138:141], v[188:191], v[34:49]
	v_exp_f32_e32 v188, v105
	v_exp_f32_e32 v189, v106
	v_exp_f32_e32 v190, v107
	v_exp_f32_e32 v191, v108
	v_mfma_f32_32x32x16_bf16 v[18:33], v[138:141], v[222:225], v[18:33]
	v_mfma_f32_32x32x16_bf16 v[34:49], v[142:145], v[192:195], v[34:49]
	v_exp_f32_e32 v192, v109
	v_exp_f32_e32 v193, v110
	v_exp_f32_e32 v194, v111
	v_exp_f32_e32 v195, v112
	v_mfma_f32_32x32x16_bf16 v[18:33], v[142:145], v[226:229], v[18:33]
	s_andn2_b64 vcc, exec, s[24:25]
	s_cbranch_vccz .LBB0_866

; #define DMA_WAIT(last) do { if (last) asm volatile("s_waitcnt vmcnt(0)" ::: "memory"); else asm volatile("s_waitcnt vmcnt(%0)" :: "n"(NPW) : "memory"); } while (0)
; template <int DK, int DV, bool OFF, class QLoader> ...
;     ...
;   f32x16 pA0, pA1, pB0, pB1; bf16x8 pa0, pa1, pa2, pa3; const int NT = nkeys / KVBLK;
;   DMA_TILE(0, 0); DMA_TILE(1, 1); DMA_WAIT(false); __syncthreads(); if (2 < NT) DMA_TILE(2, 2);
;   qkt<DK>(pA0, pA1, K_lds, qr, r32, hi); partialSM<DK, OFF>(pA0, pA1, negMC);
.LBB0_868:
.LBB0_870:
	s_add_i32 s24, s55, -1
	s_cmp_ge_u32 s24, s95
	s_waitcnt vmcnt(0)
	s_barrier
	s_cbranch_scc1 .LBB0_872
	v_lshl_add_u64 v[82:83], v[156:157], 0, s[8:9]
	s_mov_b64 s[24:25], 0x1ec0a000
	s_mov_b32 m0, s85
	v_lshl_add_u64 v[82:83], v[82:83], 0, s[24:25]
	global_load_lds_dwordx4 v[82:83], off
	v_lshl_add_u64 v[82:83], v[154:155], 0, s[8:9]
	s_mov_b64 s[24:25], 0x1ec0a200
	v_lshl_add_u64 v[82:83], v[82:83], 0, s[24:25]
	s_mov_b32 m0, s86
	s_mov_b64 s[24:25], 0xdc61000
	global_load_lds_dwordx4 v[82:83], off
	v_lshl_add_u64 v[82:83], v[152:153], 0, s[8:9]
	v_lshl_add_u64 v[84:85], v[82:83], 0, s[24:25]
	s_mov_b32 m0, s87
	s_mov_b64 s[24:25], 0xdc61080
	global_load_lds_dwordx4 v[84:85], off
	v_lshl_add_u64 v[82:83], v[82:83], 0, s[24:25]
	s_mov_b32 m0, s88
	s_nop 0
	global_load_lds_dwordx4 v[82:83], off
; template <int DK>
; __device__ __forceinline__ void qkt(f32x16& p0, f32x16& p1, const char* Ks, const bf16x8* qr, int r32, int hi) {
;   p0 = f32x16{}; p1 = f32x16{};
; #pragma unroll
;   for (int d0 = 0; d0 < DK / 16; ++d0) { const int cb = (d0 * 16 + hi * 8) * 2;
;     const bf16x8 b0 = *reinterpret_cast<const bf16x8*>(Ks + ATT_KSWZ(r32, cb));
;     const bf16x8 b1 = *reinterpret_cast<const bf16x8*>(Ks + ATT_KSWZ(32 + r32, cb));
;     p0 = __builtin_amdgcn_mfma_f32_32x32x16_bf16(b0, qr[d0], p0, 0, 0, 0);
;     p1 = __builtin_amdgcn_mfma_f32_32x32x16_bf16(b1, qr[d0], p1, 0, 0, 0);
;   }
; }
.LBB0_872:
	ds_read_b128 v[82:85], v162 offset:49152
	ds_read_b128 v[86:89], v162 offset:57344
	ds_read_b128 v[130:133], v164 offset:49152
	ds_read_b128 v[134:137], v164 offset:57344
	v_exp_f32_e32 v66, v66
	v_add_f32_e32 v180, 0, v173
	v_add_f32_e32 v180, v174, v180
	v_add_f32_e32 v180, v175, v180
	v_add_f32_e32 v180, v184, v180
	v_add_f32_e32 v180, v185, v180
	v_add_f32_e32 v180, v186, v180
	v_add_f32_e32 v180, v187, v180
	v_add_f32_e32 v180, v188, v180
	v_add_f32_e32 v180, v189, v180
	v_add_f32_e32 v180, v190, v180
	v_add_f32_e32 v180, v191, v180
	v_add_f32_e32 v180, v192, v180
	v_add_f32_e32 v180, v193, v180
	v_add_f32_e32 v180, v194, v180
	v_add_f32_e32 v180, v195, v180
	v_add_f32_e32 v180, v196, v180
	s_waitcnt lgkmcnt(0)
	v_mfma_f32_32x32x16_bf16 v[98:113], v[82:85], v[114:117], 0
	v_exp_f32_e32 v67, v67
	v_exp_f32_e32 v68, v68
	v_exp_f32_e32 v69, v69
	v_exp_f32_e32 v70, v70
	v_exp_f32_e32 v71, v71
	v_exp_f32_e32 v72, v72
	v_exp_f32_e32 v73, v73
	v_mfma_f32_32x32x16_bf16 v[82:97], v[86:89], v[114:117], 0
	v_exp_f32_e32 v74, v74
	v_exp_f32_e32 v75, v75
	v_exp_f32_e32 v76, v76
	v_exp_f32_e32 v77, v77
	v_exp_f32_e32 v78, v78
	v_exp_f32_e32 v79, v79
	v_exp_f32_e32 v80, v80
	v_mfma_f32_32x32x16_bf16 v[98:113], v[130:133], v[118:121], v[98:113]
	v_exp_f32_e32 v81, v81
	v_mfma_f32_32x32x16_bf16 v[82:97], v[134:137], v[118:121], v[82:97]
	ds_read_b128 v[130:133], v166 offset:49152
	ds_read_b128 v[134:137], v166 offset:57344
	v_add_f32_e32 v180, v66, v180
	v_add_f32_e32 v180, v67, v180
	v_add_f32_e32 v180, v68, v180
	v_add_f32_e32 v180, v69, v180
	v_add_f32_e32 v180, v70, v180
	v_add_f32_e32 v180, v71, v180
	v_add_f32_e32 v180, v72, v180
	v_add_f32_e32 v180, v73, v180
	s_waitcnt lgkmcnt(0)
	v_mfma_f32_32x32x16_bf16 v[98:113], v[130:133], v[122:125], v[98:113]
	v_mfma_f32_32x32x16_bf16 v[82:97], v[134:137], v[122:125], v[82:97]
	ds_read_b128 v[130:133], v168 offset:49152
	ds_read_b128 v[134:137], v168 offset:57344
	v_add_f32_e32 v180, v74, v180
	v_add_f32_e32 v180, v75, v180
	v_add_f32_e32 v180, v76, v180
	v_add_f32_e32 v180, v77, v180
	v_add_f32_e32 v180, v78, v180
	v_add_f32_e32 v180, v79, v180
	v_add_f32_e32 v180, v80, v180
	v_add_f32_e32 v180, v81, v180
	s_waitcnt lgkmcnt(0)
	v_mfma_f32_32x32x16_bf16 v[98:113], v[130:133], v[126:129], v[98:113]
	v_mfma_f32_32x32x16_bf16 v[82:97], v[134:137], v[126:129], v[82:97]
	v_add_f32_e32 v172, v172, v180
	v_cvt_pk_bf16_f32 v130, v173, v174
	v_cvt_pk_bf16_f32 v131, v175, v184
	v_cvt_pk_bf16_f32 v132, v185, v186
	v_cvt_pk_bf16_f32 v133, v187, v188
	v_cvt_pk_bf16_f32 v134, v189, v190
	v_cvt_pk_bf16_f32 v135, v191, v192
	v_cvt_pk_bf16_f32 v136, v193, v194
	v_cvt_pk_bf16_f32 v137, v195, v196
	v_cvt_pk_bf16_f32 v138, v66, v67
	v_cvt_pk_bf16_f32 v139, v68, v69
	v_cvt_pk_bf16_f32 v140, v70, v71
	v_cvt_pk_bf16_f32 v141, v72, v73
	v_cvt_pk_bf16_f32 v142, v74, v75
	v_cvt_pk_bf16_f32 v143, v76, v77
	v_cvt_pk_bf16_f32 v144, v78, v79
	v_cvt_pk_bf16_f32 v145, v80, v81
	ds_read_b64_tr_b16 v[176:177], v171 offset:0
	ds_read_b64_tr_b16 v[178:179], v171 offset:0x800
	ds_read_b64_tr_b16 v[198:199], v171 offset:0x1000
	ds_read_b64_tr_b16 v[200:201], v171 offset:0x1800
	ds_read_b64_tr_b16 v[202:203], v171 offset:0x2000
	ds_read_b64_tr_b16 v[204:205], v171 offset:0x2800
	ds_read_b64_tr_b16 v[206:207], v171 offset:0x3000
	ds_read_b64_tr_b16 v[208:209], v171 offset:0x3800
	ds_read_b64_tr_b16 v[210:211], v171 offset:0x200
	ds_read_b64_tr_b16 v[212:213], v171 offset:0xa00
	ds_read_b64_tr_b16 v[214:215], v171 offset:0x1200
	s_nop 0
	v_permlane32_swap_b32_e32 v130, v132
	v_permlane32_swap_b32_e32 v131, v133
	ds_read_b64_tr_b16 v[216:217], v171 offset:0x1a00
	ds_read_b64_tr_b16 v[218:219], v171 offset:0x2200
	ds_read_b64_tr_b16 v[220:221], v171 offset:0x2a00
	ds_read_b64_tr_b16 v[222:223], v171 offset:0x3200
	ds_read_b64_tr_b16 v[224:225], v171 offset:0x3a00
	s_waitcnt lgkmcnt(8)
	v_permlane32_swap_b32_e32 v134, v136
	s_nop 0
	v_mfma_f32_32x32x16_bf16 v[2:17], v[130:133], v[176:179], v[2:17]
	v_permlane32_swap_b32_e32 v135, v137
	v_permlane32_swap_b32_e32 v138, v140
	v_permlane32_swap_b32_e32 v139, v141
	ds_read_b64_tr_b16 v[176:177], v171 offset:0x400
	v_mfma_f32_32x32x16_bf16 v[2:17], v[134:137], v[198:201], v[2:17]
	v_permlane32_swap_b32_e32 v142, v144
	v_permlane32_swap_b32_e32 v143, v145
	ds_read_b64_tr_b16 v[178:179], v171 offset:0xc00
	ds_read_b64_tr_b16 v[198:199], v171 offset:0x1400
	ds_read_b64_tr_b16 v[200:201], v171 offset:0x1c00
	v_mfma_f32_32x32x16_bf16 v[2:17], v[138:141], v[202:205], v[2:17]
	ds_read_b64_tr_b16 v[202:203], v171 offset:0x2400
	ds_read_b64_tr_b16 v[204:205], v171 offset:0x2c00
	v_exp_f32_e32 v197, v98
	v_mfma_f32_32x32x16_bf16 v[2:17], v[142:145], v[206:209], v[2:17]
	ds_read_b64_tr_b16 v[206:207], v171 offset:0x3400
	ds_read_b64_tr_b16 v[208:209], v171 offset:0x3c00
	s_waitcnt lgkmcnt(8)
	s_nop 0
	v_mfma_f32_32x32x16_bf16 v[50:65], v[130:133], v[210:213], v[50:65]
	ds_read_b64_tr_b16 v[210:211], v171 offset:0x600
	ds_read_b64_tr_b16 v[212:213], v171 offset:0xe00
	v_mfma_f32_32x32x16_bf16 v[50:65], v[134:137], v[214:217], v[50:65]
	ds_read_b64_tr_b16 v[214:215], v171 offset:0x1600
	ds_read_b64_tr_b16 v[216:217], v171 offset:0x1e00
	v_mfma_f32_32x32x16_bf16 v[50:65], v[138:141], v[218:221], v[50:65]
	ds_read_b64_tr_b16 v[218:219], v171 offset:0x2600
	ds_read_b64_tr_b16 v[220:221], v171 offset:0x2e00
	v_mfma_f32_32x32x16_bf16 v[50:65], v[142:145], v[222:225], v[50:65]
	ds_read_b64_tr_b16 v[222:223], v171 offset:0x3600
	ds_read_b64_tr_b16 v[224:225], v171 offset:0x3e00
	s_waitcnt lgkmcnt(8)
	s_nop 0
	s_waitcnt lgkmcnt(0)
	v_mfma_f32_32x32x16_bf16 v[34:49], v[130:133], v[176:179], v[34:49]
	v_mfma_f32_32x32x16_bf16 v[18:33], v[130:133], v[210:213], v[18:33]
	v_exp_f32_e32 v210, v105
	v_exp_f32_e32 v211, v111
	v_exp_f32_e32 v212, v113
	v_mfma_f32_32x32x16_bf16 v[34:49], v[134:137], v[198:201], v[34:49]
	v_exp_f32_e32 v200, v99
	v_exp_f32_e32 v198, v100
	v_exp_f32_e32 v199, v106
	v_exp_f32_e32 v201, v108
	v_mfma_f32_32x32x16_bf16 v[18:33], v[134:137], v[214:217], v[18:33]
	v_mfma_f32_32x32x16_bf16 v[34:49], v[138:141], v[202:205], v[34:49]
	v_exp_f32_e32 v202, v101
	v_exp_f32_e32 v204, v102
	v_exp_f32_e32 v205, v104
	v_exp_f32_e32 v203, v107
	v_mfma_f32_32x32x16_bf16 v[18:33], v[138:141], v[218:221], v[18:33]
	v_mfma_f32_32x32x16_bf16 v[34:49], v[142:145], v[206:209], v[34:49]
	v_exp_f32_e32 v207, v103
	v_exp_f32_e32 v209, v109
	v_exp_f32_e32 v206, v110
	v_exp_f32_e32 v208, v112
	v_mfma_f32_32x32x16_bf16 v[18:33], v[142:145], v[222:225], v[18:33]
	s_cmp_ge_u32 s57, s97
	s_cbranch_scc1 .LBB0_880

; #define DMA_WAIT(last) do { if (last) asm volatile("s_waitcnt vmcnt(0)" ::: "memory"); else asm volatile("s_waitcnt vmcnt(%0)" :: "n"(NPW) : "memory"); } while (0)
; template <int DK, int DV, bool OFF, class QLoader> ...
;     ...
;   f32x16 pA0, pA1, pB0, pB1; bf16x8 pa0, pa1, pa2, pa3; const int NT = nkeys / KVBLK;
;   DMA_TILE(0, 0); DMA_TILE(1, 1); DMA_WAIT(false); __syncthreads(); if (2 < NT) DMA_TILE(2, 2);
;   qkt<DK>(pA0, pA1, K_lds, qr, r32, hi); partialSM<DK, OFF>(pA0, pA1, negMC);
.LBB0_875:
.LBB0_877:
	s_cmp_ge_u32 s55, s95
	s_waitcnt vmcnt(0)
	s_barrier
	s_cbranch_scc1 .LBB0_879
	v_lshl_add_u64 v[66:67], v[156:157], 0, s[8:9]
	s_mov_b64 s[24:25], 0x1ec0c000
	s_mov_b32 m0, s89
	v_lshl_add_u64 v[66:67], v[66:67], 0, s[24:25]
	global_load_lds_dwordx4 v[66:67], off
	v_lshl_add_u64 v[66:67], v[154:155], 0, s[8:9]
	s_mov_b64 s[24:25], 0x1ec0c200
	v_lshl_add_u64 v[66:67], v[66:67], 0, s[24:25]
	s_mov_b32 m0, s90
	s_mov_b64 s[24:25], 0xdcc1000
	global_load_lds_dwordx4 v[66:67], off
	v_lshl_add_u64 v[66:67], v[152:153], 0, s[8:9]
	v_lshl_add_u64 v[68:69], v[66:67], 0, s[24:25]
	s_mov_b32 m0, s91
	s_mov_b64 s[24:25], 0xdcc1080
	global_load_lds_dwordx4 v[68:69], off
	v_lshl_add_u64 v[66:67], v[66:67], 0, s[24:25]
	s_mov_b32 m0, s92
	s_nop 0
	global_load_lds_dwordx4 v[66:67], off

; #define DMA_WAIT(last) do { if (last) asm volatile("s_waitcnt vmcnt(0)" ::: "memory"); else asm volatile("s_waitcnt vmcnt(%0)" :: "n"(NPW) : "memory"); } while (0)
; template <int DK, int DV, bool OFF, class QLoader> ...
;     ...
;   f32x16 pA0, pA1, pB0, pB1; bf16x8 pa0, pa1, pa2, pa3; const int NT = nkeys / KVBLK;
;   DMA_TILE(0, 0); DMA_TILE(1, 1); DMA_WAIT(false); __syncthreads(); if (2 < NT) DMA_TILE(2, 2);
;   qkt<DK>(pA0, pA1, K_lds, qr, r32, hi); partialSM<DK, OFF>(pA0, pA1, negMC);
.LBB0_1436:
.LBB0_1438:
	s_add_i32 s40, s92, 2
	s_cmp_lt_u32 s40, s89
	s_cselect_b64 s[0:1], -1, 0
	s_cmp_ge_u32 s40, s89
	s_cselect_b64 s[40:41], -1, 0
	s_and_b64 vcc, exec, s[40:41]
	s_waitcnt vmcnt(0)
	s_barrier
	s_cbranch_vccnz .LBB0_1440
	v_lshl_add_u64 v[34:35], v[92:93], 0, s[12:13]
	s_mov_b64 s[94:95], 0x2a815000
	s_mov_b32 m0, s85
	v_lshl_add_u64 v[34:35], v[34:35], 0, s[94:95]
	global_load_lds_dwordx4 v[34:35], off
	v_lshl_add_u64 v[34:35], v[94:95], 0, s[12:13]
	v_lshl_add_u64 v[34:35], v[34:35], 0, s[94:95]
	s_mov_b32 m0, s86
	s_mov_b64 s[94:95], 0x30e0e000
	global_load_lds_dwordx4 v[34:35], off
	v_lshl_add_u64 v[34:35], v[90:91], 0, s[12:13]
	v_lshl_add_u64 v[34:35], v[34:35], 0, s[94:95]
	s_mov_b32 m0, s88
	s_nop 0
	global_load_lds_dwordx4 v[34:35], off

; #define DMA_WAIT(last) do { if (last) asm volatile("s_waitcnt vmcnt(0)" ::: "memory"); else asm volatile("s_waitcnt vmcnt(%0)" :: "n"(NPW) : "memory"); } while (0)
; template <int DK, int DV, bool OFF, class QLoader> ...
;     ...
;   f32x16 pA0, pA1, pB0, pB1; bf16x8 pa0, pa1, pa2, pa3; const int NT = nkeys / KVBLK;
;   DMA_TILE(0, 0); DMA_TILE(1, 1); DMA_WAIT(false); __syncthreads(); if (2 < NT) DMA_TILE(2, 2);
;   qkt<DK>(pA0, pA1, K_lds, qr, r32, hi); partialSM<DK, OFF>(pA0, pA1, negMC);
.LBB0_1443:
.LBB0_1445:
	s_add_i32 s38, s92, 3
	s_cmp_ge_u32 s38, s89
	s_waitcnt vmcnt(0)
	s_barrier
	s_cbranch_scc1 .LBB0_1447
	v_lshl_add_u64 v[50:51], v[92:93], 0, s[12:13]
	s_mov_b64 s[38:39], 0x2a818000
	s_mov_b32 m0, s81
	v_lshl_add_u64 v[50:51], v[50:51], 0, s[38:39]
	global_load_lds_dwordx4 v[50:51], off
	v_lshl_add_u64 v[50:51], v[94:95], 0, s[12:13]
	v_lshl_add_u64 v[50:51], v[50:51], 0, s[38:39]
	s_mov_b32 m0, s82
	s_mov_b64 s[38:39], 0x30e10000
	global_load_lds_dwordx4 v[50:51], off
	v_lshl_add_u64 v[50:51], v[90:91], 0, s[12:13]
	v_lshl_add_u64 v[50:51], v[50:51], 0, s[38:39]
	s_mov_b32 m0, s87
	s_nop 0
	global_load_lds_dwordx4 v[50:51], off

; #define DMA_WAIT(last) do { if (last) asm volatile("s_waitcnt vmcnt(0)" ::: "memory"); else asm volatile("s_waitcnt vmcnt(%0)" :: "n"(NPW) : "memory"); } while (0)
; template <int DK, int DV, bool OFF, class QLoader> ...
;     ...
;   f32x16 pA0, pA1, pB0, pB1; bf16x8 pa0, pa1, pa2, pa3; const int NT = nkeys / KVBLK;
;   DMA_TILE(0, 0); DMA_TILE(1, 1); DMA_WAIT(false); __syncthreads(); if (2 < NT) DMA_TILE(2, 2);
;   qkt<DK>(pA0, pA1, K_lds, qr, r32, hi); partialSM<DK, OFF>(pA0, pA1, negMC);
.LBB0_1452:
.LBB0_1454:
	s_add_i32 s0, s92, 4
	s_cmp_ge_u32 s0, s89
	s_waitcnt vmcnt(0)
	s_barrier
	s_cbranch_scc1 .LBB0_1456
	v_lshl_add_u64 v[34:35], v[92:93], 0, s[12:13]
	s_mov_b64 s[0:1], 0x2a81b000
	s_mov_b32 m0, s83
	v_lshl_add_u64 v[34:35], v[34:35], 0, s[0:1]
	global_load_lds_dwordx4 v[34:35], off
	v_lshl_add_u64 v[34:35], v[94:95], 0, s[12:13]
	v_lshl_add_u64 v[34:35], v[34:35], 0, s[0:1]
	s_mov_b32 m0, s84
	s_mov_b64 s[0:1], 0x30e12000
	global_load_lds_dwordx4 v[34:35], off
	v_lshl_add_u64 v[34:35], v[90:91], 0, s[12:13]
	v_lshl_add_u64 v[34:35], v[34:35], 0, s[0:1]
	s_add_i32 m0, s87, 0x2000
	s_nop 0
	global_load_lds_dwordx4 v[34:35], off

; #define DMA_WAIT(last) do { if (last) asm volatile("s_waitcnt vmcnt(0)" ::: "memory"); else asm volatile("s_waitcnt vmcnt(%0)" :: "n"(NPW) : "memory"); } while (0)
; template <int DK, int DV, bool OFF, class QLoader> ...
;     ...
;   f32x16 pA0, pA1, pB0, pB1; bf16x8 pa0, pa1, pa2, pa3; const int NT = nkeys / KVBLK;
;   DMA_TILE(0, 0); DMA_TILE(1, 1); DMA_WAIT(false); __syncthreads(); if (2 < NT) DMA_TILE(2, 2);
;   qkt<DK>(pA0, pA1, K_lds, qr, r32, hi); partialSM<DK, OFF>(pA0, pA1, negMC);
.LBB0_1459:
.LBB0_1461:
	s_add_i32 s0, s92, 5
	s_cmp_ge_u32 s0, s89
	s_waitcnt vmcnt(0)
	s_barrier
	s_cbranch_scc1 .LBB0_1432
	v_lshl_add_u64 v[50:51], v[92:93], 0, s[12:13]
	s_mov_b64 s[0:1], 0x2a81e000
	v_lshl_add_u64 v[50:51], v[50:51], 0, s[0:1]
	s_add_i32 m0, s81, 0x8000
	s_nop 0
	global_load_lds_dwordx4 v[50:51], off
	v_lshl_add_u64 v[50:51], v[94:95], 0, s[12:13]
	v_lshl_add_u64 v[50:51], v[50:51], 0, s[0:1]
	s_add_i32 m0, s81, 0x8400
	s_mov_b64 s[0:1], 0x30e14000
	global_load_lds_dwordx4 v[50:51], off
	v_lshl_add_u64 v[50:51], v[90:91], 0, s[12:13]
	v_lshl_add_u64 v[50:51], v[50:51], 0, s[0:1]
	s_add_i32 m0, s87, 0x4000
	s_nop 0
	global_load_lds_dwordx4 v[50:51], off
	s_branch .LBB0_1432
